# MoE down GEMM epilogue: GATE loads of all 8 row blocks issued up front (both layers)
# baseline (speedup 1.0000x reference)
.LBB0_1455:
	s_nop 7
	s_nop 7
	s_nop 7
	v_lshl_add_u32 v6, s50, 8, v1
	v_ashrrev_i32_e32 v7, 31, v6
	v_lshl_add_u64 v[4:5], v[6:7], 2, s[96:97]
	global_load_dword v2, v[4:5], off
	global_load_dword v241, v[4:5], off offset:64
	global_load_dword v242, v[4:5], off offset:128
	global_load_dword v243, v[4:5], off offset:192
	global_load_dword v244, v[4:5], off offset:512
	global_load_dword v245, v[4:5], off offset:576
	global_load_dword v246, v[4:5], off offset:640
	global_load_dword v247, v[4:5], off offset:704
	s_lshl_b32 s16, s33, 8
	s_and_b32 s16, s16, 0x300
	v_or_b32_e32 v8, s16, v168
	v_readlane_b32 s16, v252, 13
	v_readlane_b32 s17, v252, 14
	v_lshlrev_b32_e32 v154, 1, v8
	s_mov_b32 s33, s48
	s_mov_b32 s50, s49
	s_mov_b64 s[18:19], s[4:5]
	s_waitcnt vmcnt(7)
	v_mul_f32_e32 v12, 0x3a800000, v2
	v_lshlrev_b64 v[2:3], 11, v[6:7]
	v_lshl_add_u64 v[2:3], s[16:17], 0, v[2:3]
	v_pk_mul_f32 v[10:11], v[144:145], v[12:13] op_sel_hi:[1,0]
	v_pk_mul_f32 v[8:9], v[142:143], v[12:13] op_sel_hi:[1,0]
	v_pk_mul_f32 v[14:15], v[140:141], v[12:13] op_sel_hi:[1,0]
	v_pk_mul_f32 v[16:17], v[138:139], v[12:13] op_sel_hi:[1,0]
	v_lshl_add_u64 v[2:3], v[2:3], 0, v[154:155]
	v_cvt_pk_bf16_f32 v8, v8, v9
	v_cvt_pk_bf16_f32 v9, v10, v11
	v_cvt_pk_bf16_f32 v10, v16, v17
	v_cvt_pk_bf16_f32 v11, v14, v15
	global_store_dwordx4 v[2:3], v[8:11], off
	v_pk_mul_f32 v[14:15], v[132:133], v[12:13] op_sel_hi:[1,0]
	s_nop 0
	v_pk_mul_f32 v[10:11], v[136:137], v[12:13] op_sel_hi:[1,0]
	v_pk_mul_f32 v[8:9], v[134:135], v[12:13] op_sel_hi:[1,0]
	v_pk_mul_f32 v[12:13], v[130:131], v[12:13] op_sel_hi:[1,0]
	v_cvt_pk_bf16_f32 v8, v8, v9
	v_cvt_pk_bf16_f32 v9, v10, v11
	v_cvt_pk_bf16_f32 v10, v12, v13
	v_cvt_pk_bf16_f32 v11, v14, v15
	global_store_dwordx4 v[2:3], v[8:11], off offset:256
	s_nop 1
	v_or_b32_e32 v8, 16, v6
	v_ashrrev_i32_e32 v9, 31, v8
	v_lshl_add_u64 v[10:11], v[8:9], 2, s[96:97]
	v_lshlrev_b64 v[8:9], 11, v[8:9]
	v_lshl_add_u64 v[8:9], s[16:17], 0, v[8:9]
	v_lshl_add_u64 v[14:15], v[8:9], 0, v[154:155]
	s_waitcnt vmcnt(8)
	v_mov_b32_e32 v7, v241
	v_mul_f32_e32 v12, 0x3a800000, v7
	v_pk_mul_f32 v[10:11], v[128:129], v[12:13] op_sel_hi:[1,0]
	v_pk_mul_f32 v[8:9], v[126:127], v[12:13] op_sel_hi:[1,0]
	v_pk_mul_f32 v[16:17], v[124:125], v[12:13] op_sel_hi:[1,0]
	v_pk_mul_f32 v[122:123], v[122:123], v[12:13] op_sel_hi:[1,0]
	v_cvt_pk_bf16_f32 v8, v8, v9
	v_cvt_pk_bf16_f32 v9, v10, v11
	v_cvt_pk_bf16_f32 v10, v122, v123
	v_cvt_pk_bf16_f32 v11, v16, v17
	global_store_dwordx4 v[14:15], v[8:11], off
	v_pk_mul_f32 v[16:17], v[116:117], v[12:13] op_sel_hi:[1,0]
	s_nop 0
	v_pk_mul_f32 v[10:11], v[120:121], v[12:13] op_sel_hi:[1,0]
	v_pk_mul_f32 v[8:9], v[118:119], v[12:13] op_sel_hi:[1,0]
	v_pk_mul_f32 v[12:13], v[114:115], v[12:13] op_sel_hi:[1,0]
	v_cvt_pk_bf16_f32 v8, v8, v9
	v_cvt_pk_bf16_f32 v9, v10, v11
	v_cvt_pk_bf16_f32 v10, v12, v13
	v_cvt_pk_bf16_f32 v11, v16, v17
	global_store_dwordx4 v[14:15], v[8:11], off offset:256
	s_nop 1
	v_or_b32_e32 v8, 32, v6
	v_ashrrev_i32_e32 v9, 31, v8
	v_lshl_add_u64 v[10:11], v[8:9], 2, s[96:97]
	v_lshlrev_b64 v[8:9], 11, v[8:9]
	v_lshl_add_u64 v[8:9], s[16:17], 0, v[8:9]
	v_lshl_add_u64 v[14:15], v[8:9], 0, v[154:155]
	v_or_b32_e32 v6, 48, v6
	s_waitcnt vmcnt(9)
	v_mov_b32_e32 v7, v242
	v_mul_f32_e32 v12, 0x3a800000, v7
	v_pk_mul_f32 v[10:11], v[112:113], v[12:13] op_sel_hi:[1,0]
	v_pk_mul_f32 v[8:9], v[110:111], v[12:13] op_sel_hi:[1,0]
	v_pk_mul_f32 v[16:17], v[108:109], v[12:13] op_sel_hi:[1,0]
	v_pk_mul_f32 v[106:107], v[106:107], v[12:13] op_sel_hi:[1,0]
	v_cvt_pk_bf16_f32 v8, v8, v9
	v_cvt_pk_bf16_f32 v9, v10, v11
	v_cvt_pk_bf16_f32 v10, v106, v107
	v_cvt_pk_bf16_f32 v11, v16, v17
	global_store_dwordx4 v[14:15], v[8:11], off
	v_pk_mul_f32 v[16:17], v[100:101], v[12:13] op_sel_hi:[1,0]
	v_ashrrev_i32_e32 v7, 31, v6
	v_pk_mul_f32 v[10:11], v[104:105], v[12:13] op_sel_hi:[1,0]
	v_pk_mul_f32 v[8:9], v[102:103], v[12:13] op_sel_hi:[1,0]
	v_pk_mul_f32 v[12:13], v[98:99], v[12:13] op_sel_hi:[1,0]
	v_cvt_pk_bf16_f32 v8, v8, v9
	v_cvt_pk_bf16_f32 v9, v10, v11
	v_cvt_pk_bf16_f32 v10, v12, v13
	v_cvt_pk_bf16_f32 v11, v16, v17
	global_store_dwordx4 v[14:15], v[8:11], off offset:256
	s_nop 1
	v_lshl_add_u64 v[8:9], v[6:7], 2, s[96:97]
	v_lshlrev_b64 v[6:7], 11, v[6:7]
	v_lshl_add_u64 v[6:7], s[16:17], 0, v[6:7]
	v_lshl_add_u64 v[12:13], v[6:7], 0, v[154:155]
	s_mov_b64 s[16:17], 0x40000
	s_waitcnt vmcnt(10)
	v_mov_b32_e32 v8, v243
	v_mul_f32_e32 v10, 0x3a800000, v8
	v_pk_mul_f32 v[8:9], v[96:97], v[10:11] op_sel_hi:[1,0]
	v_pk_mul_f32 v[6:7], v[94:95], v[10:11] op_sel_hi:[1,0]
	v_pk_mul_f32 v[14:15], v[92:93], v[10:11] op_sel_hi:[1,0]
	v_pk_mul_f32 v[16:17], v[90:91], v[10:11] op_sel_hi:[1,0]
	v_cvt_pk_bf16_f32 v6, v6, v7
	v_cvt_pk_bf16_f32 v7, v8, v9
	v_cvt_pk_bf16_f32 v8, v16, v17
	v_cvt_pk_bf16_f32 v9, v14, v15
	global_store_dwordx4 v[12:13], v[6:9], off
	v_pk_mul_f32 v[14:15], v[84:85], v[10:11] op_sel_hi:[1,0]
	s_nop 0
	v_pk_mul_f32 v[8:9], v[88:89], v[10:11] op_sel_hi:[1,0]
	v_pk_mul_f32 v[6:7], v[86:87], v[10:11] op_sel_hi:[1,0]
	v_pk_mul_f32 v[10:11], v[82:83], v[10:11] op_sel_hi:[1,0]
	v_cvt_pk_bf16_f32 v6, v6, v7
	v_cvt_pk_bf16_f32 v7, v8, v9
	v_cvt_pk_bf16_f32 v8, v10, v11
	v_cvt_pk_bf16_f32 v9, v14, v15
	global_store_dwordx4 v[12:13], v[6:9], off offset:256
	v_lshl_add_u64 v[12:13], v[2:3], 0, s[16:17]
	s_mov_b32 s16, 0x40000
	s_waitcnt vmcnt(11)
	v_mov_b32_e32 v6, v244
	v_mul_f32_e32 v10, 0x3a800000, v6
	v_pk_mul_f32 v[8:9], v[80:81], v[10:11] op_sel_hi:[1,0]
	v_pk_mul_f32 v[6:7], v[78:79], v[10:11] op_sel_hi:[1,0]
	v_pk_mul_f32 v[14:15], v[76:77], v[10:11] op_sel_hi:[1,0]
	v_pk_mul_f32 v[16:17], v[74:75], v[10:11] op_sel_hi:[1,0]
	v_cvt_pk_bf16_f32 v6, v6, v7
	v_cvt_pk_bf16_f32 v7, v8, v9
	v_cvt_pk_bf16_f32 v9, v14, v15
	v_add_co_u32_e32 v14, vcc, s16, v2
	v_cvt_pk_bf16_f32 v8, v16, v17
	s_nop 0
	v_addc_co_u32_e32 v15, vcc, 0, v3, vcc
	global_store_dwordx4 v[14:15], v[6:9], off
	v_pk_mul_f32 v[14:15], v[68:69], v[10:11] op_sel_hi:[1,0]
	s_mov_b64 s[16:17], 0x48000
	v_pk_mul_f32 v[8:9], v[72:73], v[10:11] op_sel_hi:[1,0]
	v_pk_mul_f32 v[6:7], v[70:71], v[10:11] op_sel_hi:[1,0]
	v_pk_mul_f32 v[10:11], v[66:67], v[10:11] op_sel_hi:[1,0]
	v_cvt_pk_bf16_f32 v6, v6, v7
	v_cvt_pk_bf16_f32 v7, v8, v9
	v_cvt_pk_bf16_f32 v8, v10, v11
	v_cvt_pk_bf16_f32 v9, v14, v15
	global_store_dwordx4 v[12:13], v[6:9], off offset:256
	v_lshl_add_u64 v[12:13], v[2:3], 0, s[16:17]
	s_mov_b32 s16, 0x48000
	s_waitcnt vmcnt(12)
	v_mov_b32_e32 v6, v245
	v_mul_f32_e32 v10, 0x3a800000, v6
	v_pk_mul_f32 v[8:9], v[64:65], v[10:11] op_sel_hi:[1,0]
	v_pk_mul_f32 v[6:7], v[62:63], v[10:11] op_sel_hi:[1,0]
	v_pk_mul_f32 v[14:15], v[60:61], v[10:11] op_sel_hi:[1,0]
	v_pk_mul_f32 v[16:17], v[58:59], v[10:11] op_sel_hi:[1,0]
	v_cvt_pk_bf16_f32 v6, v6, v7
	v_cvt_pk_bf16_f32 v7, v8, v9
	v_cvt_pk_bf16_f32 v9, v14, v15
	v_add_co_u32_e32 v14, vcc, s16, v2
	v_cvt_pk_bf16_f32 v8, v16, v17
	s_nop 0
	v_addc_co_u32_e32 v15, vcc, 0, v3, vcc
	global_store_dwordx4 v[14:15], v[6:9], off
	v_pk_mul_f32 v[14:15], v[52:53], v[10:11] op_sel_hi:[1,0]
	s_mov_b64 s[16:17], 0x50000
	v_pk_mul_f32 v[8:9], v[56:57], v[10:11] op_sel_hi:[1,0]
	v_pk_mul_f32 v[6:7], v[54:55], v[10:11] op_sel_hi:[1,0]
	v_pk_mul_f32 v[10:11], v[50:51], v[10:11] op_sel_hi:[1,0]
	v_cvt_pk_bf16_f32 v6, v6, v7
	v_cvt_pk_bf16_f32 v7, v8, v9
	v_cvt_pk_bf16_f32 v8, v10, v11
	v_cvt_pk_bf16_f32 v9, v14, v15
	global_store_dwordx4 v[12:13], v[6:9], off offset:256
	v_lshl_add_u64 v[12:13], v[2:3], 0, s[16:17]
	s_mov_b32 s16, 0x50000
	s_waitcnt vmcnt(13)
	v_mov_b32_e32 v6, v246
	v_mul_f32_e32 v10, 0x3a800000, v6
	v_pk_mul_f32 v[8:9], v[48:49], v[10:11] op_sel_hi:[1,0]
	v_pk_mul_f32 v[6:7], v[46:47], v[10:11] op_sel_hi:[1,0]
	v_pk_mul_f32 v[14:15], v[44:45], v[10:11] op_sel_hi:[1,0]
	v_pk_mul_f32 v[16:17], v[42:43], v[10:11] op_sel_hi:[1,0]
	v_cvt_pk_bf16_f32 v6, v6, v7
	v_cvt_pk_bf16_f32 v7, v8, v9
	v_cvt_pk_bf16_f32 v9, v14, v15
	v_add_co_u32_e32 v14, vcc, s16, v2
	v_cvt_pk_bf16_f32 v8, v16, v17
	s_nop 0
	v_addc_co_u32_e32 v15, vcc, 0, v3, vcc
	global_store_dwordx4 v[14:15], v[6:9], off
	v_pk_mul_f32 v[14:15], v[36:37], v[10:11] op_sel_hi:[1,0]
	s_mov_b64 s[16:17], 0x58000
	v_pk_mul_f32 v[8:9], v[40:41], v[10:11] op_sel_hi:[1,0]
	v_pk_mul_f32 v[6:7], v[38:39], v[10:11] op_sel_hi:[1,0]
	v_pk_mul_f32 v[10:11], v[34:35], v[10:11] op_sel_hi:[1,0]
	v_cvt_pk_bf16_f32 v6, v6, v7
	v_cvt_pk_bf16_f32 v7, v8, v9
	v_cvt_pk_bf16_f32 v8, v10, v11
	v_cvt_pk_bf16_f32 v9, v14, v15
	global_store_dwordx4 v[12:13], v[6:9], off offset:256
	v_lshl_add_u64 v[10:11], v[2:3], 0, s[16:17]
	s_mov_b32 s16, 0x58000
	v_add_co_u32_e32 v2, vcc, s16, v2
	s_mov_b64 s[16:17], s[14:15]
	s_nop 0
	v_addc_co_u32_e32 v3, vcc, 0, v3, vcc
	s_and_b64 vcc, exec, s[12:13]
	s_waitcnt vmcnt(14)
	v_mov_b32_e32 v4, v247
	v_mul_f32_e32 v8, 0x3a800000, v4
	v_pk_mul_f32 v[6:7], v[32:33], v[8:9] op_sel_hi:[1,0]
	v_pk_mul_f32 v[4:5], v[30:31], v[8:9] op_sel_hi:[1,0]
	v_pk_mul_f32 v[12:13], v[28:29], v[8:9] op_sel_hi:[1,0]
	v_pk_mul_f32 v[14:15], v[26:27], v[8:9] op_sel_hi:[1,0]
	v_cvt_pk_bf16_f32 v4, v4, v5
	v_cvt_pk_bf16_f32 v5, v6, v7
	v_cvt_pk_bf16_f32 v6, v14, v15
	v_cvt_pk_bf16_f32 v7, v12, v13
	global_store_dwordx4 v[2:3], v[4:7], off
	v_pk_mul_f32 v[2:3], v[22:23], v[8:9] op_sel_hi:[1,0]
	s_nop 0
	v_pk_mul_f32 v[4:5], v[24:25], v[8:9] op_sel_hi:[1,0]
	v_pk_mul_f32 v[6:7], v[20:21], v[8:9] op_sel_hi:[1,0]
	v_pk_mul_f32 v[8:9], v[18:19], v[8:9] op_sel_hi:[1,0]
	v_cvt_pk_bf16_f32 v2, v2, v3
	v_cvt_pk_bf16_f32 v3, v4, v5
	v_cvt_pk_bf16_f32 v4, v8, v9
	v_cvt_pk_bf16_f32 v5, v6, v7
	global_store_dwordx4 v[10:11], v[2:5], off offset:256
	s_cbranch_vccnz .LBB0_1465

.LBB0_2715:
	s_nop 7
	s_nop 7
	s_nop 7
	v_lshl_add_u32 v14, s62, 8, v1
	v_ashrrev_i32_e32 v15, 31, v14
	v_lshl_add_u64 v[2:3], v[14:15], 2, s[96:97]
	global_load_dword v6, v[2:3], off
	global_load_dword v241, v[2:3], off offset:64
	global_load_dword v242, v[2:3], off offset:128
	global_load_dword v243, v[2:3], off offset:192
	global_load_dword v244, v[2:3], off offset:512
	global_load_dword v245, v[2:3], off offset:576
	global_load_dword v246, v[2:3], off offset:640
	global_load_dword v247, v[2:3], off offset:704
	s_lshl_b32 s24, s33, 8
	s_and_b32 s24, s24, 0x300
	v_or_b32_e32 v7, s24, v168
	v_lshlrev_b64 v[4:5], 11, v[14:15]
	v_or_b32_e32 v16, 16, v14
	v_lshl_add_u64 v[4:5], s[80:81], 0, v[4:5]
	v_lshlrev_b32_e32 v154, 1, v7
	v_ashrrev_i32_e32 v17, 31, v16
	v_lshl_add_u64 v[4:5], v[4:5], 0, v[154:155]
	v_lshl_add_u64 v[160:161], v[16:17], 2, s[96:97]
	s_mov_b64 s[26:27], s[2:3]
	s_mov_b32 s33, s60
	s_mov_b32 s62, s61
	s_mov_b64 s[24:25], s[22:23]
	s_waitcnt vmcnt(7)
	v_mul_f32_e32 v6, 0x3a800000, v6
	v_pk_mul_f32 v[8:9], v[144:145], v[6:7] op_sel_hi:[1,0]
	v_pk_mul_f32 v[10:11], v[142:143], v[6:7] op_sel_hi:[1,0]
	v_pk_mul_f32 v[12:13], v[140:141], v[6:7] op_sel_hi:[1,0]
	v_pk_mul_f32 v[138:139], v[138:139], v[6:7] op_sel_hi:[1,0]
	v_pk_mul_f32 v[136:137], v[136:137], v[6:7] op_sel_hi:[1,0]
	v_pk_mul_f32 v[134:135], v[134:135], v[6:7] op_sel_hi:[1,0]
	v_pk_mul_f32 v[132:133], v[132:133], v[6:7] op_sel_hi:[1,0]
	v_pk_mul_f32 v[130:131], v[130:131], v[6:7] op_sel_hi:[1,0]
	v_cvt_pk_bf16_f32 v6, v10, v11
	v_cvt_pk_bf16_f32 v7, v8, v9
	v_cvt_pk_bf16_f32 v8, v138, v139
	v_cvt_pk_bf16_f32 v9, v12, v13
	v_cvt_pk_bf16_f32 v10, v134, v135
	v_cvt_pk_bf16_f32 v11, v136, v137
	v_cvt_pk_bf16_f32 v12, v130, v131
	v_cvt_pk_bf16_f32 v13, v132, v133
	global_store_dwordx4 v[4:5], v[6:9], off
	global_store_dwordx4 v[4:5], v[10:13], off offset:256
	v_lshlrev_b64 v[6:7], 11, v[16:17]
	v_lshl_add_u64 v[6:7], s[80:81], 0, v[6:7]
	v_lshl_add_u64 v[132:133], v[6:7], 0, v[154:155]
	v_or_b32_e32 v130, 32, v14
	v_ashrrev_i32_e32 v131, 31, v130
	v_lshl_add_u64 v[16:17], v[130:131], 2, s[96:97]
	v_or_b32_e32 v14, 48, v14
	v_ashrrev_i32_e32 v15, 31, v14
	s_waitcnt vmcnt(8)
	v_mov_b32_e32 v8, v241
	v_mul_f32_e32 v6, 0x3a800000, v8
	v_pk_mul_f32 v[8:9], v[128:129], v[6:7] op_sel_hi:[1,0]
	v_pk_mul_f32 v[10:11], v[126:127], v[6:7] op_sel_hi:[1,0]
	v_pk_mul_f32 v[12:13], v[124:125], v[6:7] op_sel_hi:[1,0]
	v_pk_mul_f32 v[122:123], v[122:123], v[6:7] op_sel_hi:[1,0]
	v_pk_mul_f32 v[120:121], v[120:121], v[6:7] op_sel_hi:[1,0]
	v_pk_mul_f32 v[118:119], v[118:119], v[6:7] op_sel_hi:[1,0]
	v_pk_mul_f32 v[116:117], v[116:117], v[6:7] op_sel_hi:[1,0]
	v_pk_mul_f32 v[114:115], v[114:115], v[6:7] op_sel_hi:[1,0]
	v_cvt_pk_bf16_f32 v6, v10, v11
	v_cvt_pk_bf16_f32 v7, v8, v9
	v_cvt_pk_bf16_f32 v8, v122, v123
	v_cvt_pk_bf16_f32 v9, v12, v13
	v_cvt_pk_bf16_f32 v10, v118, v119
	v_cvt_pk_bf16_f32 v11, v120, v121
	v_cvt_pk_bf16_f32 v12, v114, v115
	v_cvt_pk_bf16_f32 v13, v116, v117
	global_store_dwordx4 v[132:133], v[6:9], off
	global_store_dwordx4 v[132:133], v[10:13], off offset:256
	v_lshlrev_b64 v[6:7], 11, v[130:131]
	v_lshl_add_u64 v[6:7], s[80:81], 0, v[6:7]
	v_lshl_add_u64 v[114:115], v[6:7], 0, v[154:155]
	v_lshl_add_u64 v[16:17], v[14:15], 2, s[96:97]
	s_waitcnt vmcnt(9)
	v_mov_b32_e32 v8, v242
	v_mul_f32_e32 v6, 0x3a800000, v8
	v_pk_mul_f32 v[8:9], v[112:113], v[6:7] op_sel_hi:[1,0]
	v_pk_mul_f32 v[10:11], v[110:111], v[6:7] op_sel_hi:[1,0]
	v_pk_mul_f32 v[12:13], v[108:109], v[6:7] op_sel_hi:[1,0]
	v_pk_mul_f32 v[106:107], v[106:107], v[6:7] op_sel_hi:[1,0]
	v_pk_mul_f32 v[104:105], v[104:105], v[6:7] op_sel_hi:[1,0]
	v_pk_mul_f32 v[102:103], v[102:103], v[6:7] op_sel_hi:[1,0]
	v_pk_mul_f32 v[100:101], v[100:101], v[6:7] op_sel_hi:[1,0]
	v_pk_mul_f32 v[98:99], v[98:99], v[6:7] op_sel_hi:[1,0]
	v_cvt_pk_bf16_f32 v6, v10, v11
	v_cvt_pk_bf16_f32 v7, v8, v9
	v_cvt_pk_bf16_f32 v8, v106, v107
	v_cvt_pk_bf16_f32 v9, v12, v13
	v_cvt_pk_bf16_f32 v10, v102, v103
	v_cvt_pk_bf16_f32 v11, v104, v105
	v_cvt_pk_bf16_f32 v12, v98, v99
	v_cvt_pk_bf16_f32 v13, v100, v101
	global_store_dwordx4 v[114:115], v[6:9], off
	global_store_dwordx4 v[114:115], v[10:13], off offset:256
	v_lshlrev_b64 v[6:7], 11, v[14:15]
	v_lshl_add_u64 v[6:7], s[80:81], 0, v[6:7]
	v_lshl_add_u64 v[14:15], v[6:7], 0, v[154:155]
	s_waitcnt vmcnt(10)
	v_mov_b32_e32 v8, v243
	v_mul_f32_e32 v6, 0x3a800000, v8
	v_pk_mul_f32 v[8:9], v[96:97], v[6:7] op_sel_hi:[1,0]
	v_pk_mul_f32 v[10:11], v[94:95], v[6:7] op_sel_hi:[1,0]
	v_pk_mul_f32 v[12:13], v[92:93], v[6:7] op_sel_hi:[1,0]
	v_pk_mul_f32 v[16:17], v[90:91], v[6:7] op_sel_hi:[1,0]
	v_pk_mul_f32 v[88:89], v[88:89], v[6:7] op_sel_hi:[1,0]
	v_pk_mul_f32 v[86:87], v[86:87], v[6:7] op_sel_hi:[1,0]
	v_pk_mul_f32 v[84:85], v[84:85], v[6:7] op_sel_hi:[1,0]
	v_pk_mul_f32 v[82:83], v[82:83], v[6:7] op_sel_hi:[1,0]
	v_cvt_pk_bf16_f32 v6, v10, v11
	v_cvt_pk_bf16_f32 v7, v8, v9
	v_cvt_pk_bf16_f32 v8, v16, v17
	v_cvt_pk_bf16_f32 v9, v12, v13
	v_cvt_pk_bf16_f32 v10, v86, v87
	v_cvt_pk_bf16_f32 v11, v88, v89
	v_cvt_pk_bf16_f32 v12, v82, v83
	v_cvt_pk_bf16_f32 v13, v84, v85
	global_store_dwordx4 v[14:15], v[6:9], off
	global_store_dwordx4 v[14:15], v[10:13], off offset:256
	v_add_co_u32_e32 v16, vcc, s54, v4
	v_lshl_add_u64 v[14:15], v[4:5], 0, s[12:13]
	s_nop 0
	v_addc_co_u32_e32 v17, vcc, 0, v5, vcc
	s_waitcnt vmcnt(11)
	v_mov_b32_e32 v6, v244
	v_mul_f32_e32 v6, 0x3a800000, v6
	v_pk_mul_f32 v[8:9], v[80:81], v[6:7] op_sel_hi:[1,0]
	v_pk_mul_f32 v[10:11], v[78:79], v[6:7] op_sel_hi:[1,0]
	v_pk_mul_f32 v[12:13], v[76:77], v[6:7] op_sel_hi:[1,0]
	v_pk_mul_f32 v[74:75], v[74:75], v[6:7] op_sel_hi:[1,0]
	v_pk_mul_f32 v[72:73], v[72:73], v[6:7] op_sel_hi:[1,0]
	v_pk_mul_f32 v[70:71], v[70:71], v[6:7] op_sel_hi:[1,0]
	v_pk_mul_f32 v[68:69], v[68:69], v[6:7] op_sel_hi:[1,0]
	v_pk_mul_f32 v[66:67], v[66:67], v[6:7] op_sel_hi:[1,0]
	v_cvt_pk_bf16_f32 v6, v10, v11
	v_cvt_pk_bf16_f32 v7, v8, v9
	v_cvt_pk_bf16_f32 v8, v74, v75
	v_cvt_pk_bf16_f32 v9, v12, v13
	v_cvt_pk_bf16_f32 v10, v70, v71
	v_cvt_pk_bf16_f32 v11, v72, v73
	v_cvt_pk_bf16_f32 v12, v66, v67
	v_cvt_pk_bf16_f32 v13, v68, v69
	global_store_dwordx4 v[16:17], v[6:9], off
	global_store_dwordx4 v[14:15], v[10:13], off offset:256
	v_add_co_u32_e32 v16, vcc, s55, v4
	v_lshl_add_u64 v[14:15], v[4:5], 0, s[14:15]
	s_nop 0
	v_addc_co_u32_e32 v17, vcc, 0, v5, vcc
	s_waitcnt vmcnt(12)
	v_mov_b32_e32 v6, v245
	v_mul_f32_e32 v6, 0x3a800000, v6
	v_pk_mul_f32 v[8:9], v[64:65], v[6:7] op_sel_hi:[1,0]
	v_pk_mul_f32 v[10:11], v[62:63], v[6:7] op_sel_hi:[1,0]
	v_pk_mul_f32 v[12:13], v[60:61], v[6:7] op_sel_hi:[1,0]
	v_pk_mul_f32 v[58:59], v[58:59], v[6:7] op_sel_hi:[1,0]
	v_pk_mul_f32 v[56:57], v[56:57], v[6:7] op_sel_hi:[1,0]
	v_pk_mul_f32 v[54:55], v[54:55], v[6:7] op_sel_hi:[1,0]
	v_pk_mul_f32 v[52:53], v[52:53], v[6:7] op_sel_hi:[1,0]
	v_pk_mul_f32 v[50:51], v[50:51], v[6:7] op_sel_hi:[1,0]
	v_cvt_pk_bf16_f32 v6, v10, v11
	v_cvt_pk_bf16_f32 v7, v8, v9
	v_cvt_pk_bf16_f32 v8, v58, v59
	v_cvt_pk_bf16_f32 v9, v12, v13
	v_cvt_pk_bf16_f32 v10, v54, v55
	v_cvt_pk_bf16_f32 v11, v56, v57
	v_cvt_pk_bf16_f32 v12, v50, v51
	v_cvt_pk_bf16_f32 v13, v52, v53
	global_store_dwordx4 v[16:17], v[6:9], off
	global_store_dwordx4 v[14:15], v[10:13], off offset:256
	v_add_co_u32_e32 v16, vcc, s56, v4
	v_lshl_add_u64 v[14:15], v[4:5], 0, s[16:17]
	s_nop 0
	v_addc_co_u32_e32 v17, vcc, 0, v5, vcc
	s_and_b64 vcc, exec, s[20:21]
	s_waitcnt vmcnt(13)
	v_mov_b32_e32 v6, v246
	v_mul_f32_e32 v6, 0x3a800000, v6
	v_pk_mul_f32 v[8:9], v[48:49], v[6:7] op_sel_hi:[1,0]
	v_pk_mul_f32 v[10:11], v[46:47], v[6:7] op_sel_hi:[1,0]
	v_pk_mul_f32 v[12:13], v[44:45], v[6:7] op_sel_hi:[1,0]
	v_pk_mul_f32 v[42:43], v[42:43], v[6:7] op_sel_hi:[1,0]
	v_pk_mul_f32 v[40:41], v[40:41], v[6:7] op_sel_hi:[1,0]
	v_pk_mul_f32 v[38:39], v[38:39], v[6:7] op_sel_hi:[1,0]
	v_pk_mul_f32 v[36:37], v[36:37], v[6:7] op_sel_hi:[1,0]
	v_pk_mul_f32 v[34:35], v[34:35], v[6:7] op_sel_hi:[1,0]
	v_cvt_pk_bf16_f32 v6, v10, v11
	v_cvt_pk_bf16_f32 v7, v8, v9
	v_cvt_pk_bf16_f32 v8, v42, v43
	v_cvt_pk_bf16_f32 v9, v12, v13
	v_cvt_pk_bf16_f32 v10, v38, v39
	v_cvt_pk_bf16_f32 v11, v40, v41
	v_cvt_pk_bf16_f32 v12, v34, v35
	v_cvt_pk_bf16_f32 v13, v36, v37
	global_store_dwordx4 v[16:17], v[6:9], off
	global_store_dwordx4 v[14:15], v[10:13], off offset:256
	s_waitcnt vmcnt(14)
	v_mov_b32_e32 v2, v247
	v_mul_f32_e32 v2, 0x3a800000, v2
	v_add_co_u32_e64 v12, s[2:3], s57, v4
	v_lshl_add_u64 v[10:11], v[4:5], 0, s[18:19]
	s_nop 0
	v_addc_co_u32_e64 v13, s[2:3], 0, v5, s[2:3]
	v_pk_mul_f32 v[4:5], v[32:33], v[2:3] op_sel_hi:[1,0]
	v_pk_mul_f32 v[6:7], v[30:31], v[2:3] op_sel_hi:[1,0]
	v_pk_mul_f32 v[8:9], v[28:29], v[2:3] op_sel_hi:[1,0]
	v_pk_mul_f32 v[14:15], v[26:27], v[2:3] op_sel_hi:[1,0]
	v_pk_mul_f32 v[16:17], v[24:25], v[2:3] op_sel_hi:[1,0]
	v_pk_mul_f32 v[22:23], v[22:23], v[2:3] op_sel_hi:[1,0]
	v_pk_mul_f32 v[20:21], v[20:21], v[2:3] op_sel_hi:[1,0]
	v_pk_mul_f32 v[18:19], v[18:19], v[2:3] op_sel_hi:[1,0]
	v_cvt_pk_bf16_f32 v2, v6, v7
	v_cvt_pk_bf16_f32 v3, v4, v5
	v_cvt_pk_bf16_f32 v4, v14, v15
	v_cvt_pk_bf16_f32 v5, v8, v9
	v_cvt_pk_bf16_f32 v6, v22, v23
	v_cvt_pk_bf16_f32 v7, v16, v17
	v_cvt_pk_bf16_f32 v8, v18, v19
	v_cvt_pk_bf16_f32 v9, v20, v21
	global_store_dwordx4 v[12:13], v[2:5], off
	global_store_dwordx4 v[10:11], v[6:9], off offset:256
	s_cbranch_vccnz .LBB0_2725
